# attention tile loop: K-fragment and V-fragment LDS reads kept 7 deep in a register ring around the QK and PV MFMAs (softmax VALU finished before PV) instead of one read + full LDS wait per MFMA pair
# speedup vs baseline: 1.0055x; 1.0055x over previous
; #define LAS __attribute__((address_space(3)))
; __device__ __forceinline__ f32x4 mfma16(bf16x8 a, bf16x8 b, f32x4 c) { return __builtin_amdgcn_mfma_f32_16x16x32_bf16(a, b, c, 0, 0, 0); }
; __device__ __forceinline__ void attn_wg_task(const Frame& F, int l, int task) {
;     ...
;         const int tjr = j - wch;
;         if (tjr >= 0 && tjr <= 8) {
;             const LAS unsigned char* kb = lds + A_KBUF + (j & 1) * 64 * A_KP + c * A_KP + rq * 16;
;             const LAS unsigned char* vb = lds + A_VBUF + (j & 1) * 128 * A_VP + c * A_VP + rq * 16;
;             const LAS float* rkb = (const LAS float*)(lds + A_RK) + (j & 1) * 64;
;             f32x4 sa[2][2][2];
; #pragma unroll
;             for (int g = 0; g < 2; ++g)
; #pragma unroll
;                 for (int ab = 0; ab < 2; ++ab) { f32x4 a0 = (f32x4){0.f, 0.f, 0.f, 0.f}, a1 = (f32x4){0.f, 0.f, 0.f, 0.f};
; #pragma unroll
;                     for (int ks = 0; ks < 4; ++ks) { const bf16x8 kf = *(const LAS bf16x8*)(kb + (32 * g + 16 * ab) * A_KP + ks * 64); a0 = mfma16(kf, Qf[0][ks], a0); a1 = mfma16(kf, Qf[1][ks], a1); }
;                     sa[0][g][ab] = a0; sa[1][g][ab] = a1; }
.LBB0_528:
	s_or_b64 exec, exec, s[0:1]
	s_add_i32 s5, s72, s18
	s_and_b32 s3, s18, 1
	s_cmp_gt_u32 s5, 8
	s_cbranch_scc1 .LBB0_536
	s_mul_i32 s0, s3, 0x4400
	v_add_u32_e32 v144, s0, v229
	ds_read_b128 v[164:167], v144
	ds_read_b128 v[168:171], v144 offset:4352
	ds_read_b128 v[172:175], v144 offset:64
	ds_read_b128 v[176:179], v144 offset:4416
	ds_read_b128 v[180:183], v144 offset:128
	ds_read_b128 v[194:197], v144 offset:4480
	ds_read_b128 v[198:201], v144 offset:192
	s_lshl_b32 s0, s3, 8
	s_add_i32 s4, s0, 0
	s_add_i32 s4, s4, 0x11800
	s_mov_b64 s[0:1], -1
	s_cmp_lt_u32 s5, 6
	s_waitcnt lgkmcnt(6)
	v_mfma_f32_16x16x32_bf16 v[132:135], v[164:167], v[64:67], 0
	v_mfma_f32_16x16x32_bf16 v[128:131], v[164:167], v[68:71], 0
	ds_read_b128 v[164:167], v144 offset:4544
	s_waitcnt lgkmcnt(6)
	v_mfma_f32_16x16x32_bf16 v[140:143], v[168:171], v[64:67], 0
	v_mfma_f32_16x16x32_bf16 v[136:139], v[168:171], v[68:71], 0
	ds_read_b128 v[168:171], v144 offset:8704
	s_waitcnt lgkmcnt(6)
	v_mfma_f32_16x16x32_bf16 v[132:135], v[172:175], v[72:75], v[132:135]
	v_mfma_f32_16x16x32_bf16 v[128:131], v[172:175], v[76:79], v[128:131]
	ds_read_b128 v[172:175], v144 offset:13056
	s_waitcnt lgkmcnt(6)
	v_mfma_f32_16x16x32_bf16 v[140:143], v[176:179], v[72:75], v[140:143]
	v_mfma_f32_16x16x32_bf16 v[136:139], v[176:179], v[76:79], v[136:139]
	ds_read_b128 v[176:179], v144 offset:8768
	s_waitcnt lgkmcnt(6)
	v_mfma_f32_16x16x32_bf16 v[132:135], v[180:183], v[80:83], v[132:135]
	v_mfma_f32_16x16x32_bf16 v[128:131], v[180:183], v[84:87], v[128:131]
	ds_read_b128 v[180:183], v144 offset:13120
	s_waitcnt lgkmcnt(6)
	v_mfma_f32_16x16x32_bf16 v[140:143], v[194:197], v[80:83], v[140:143]
	v_mfma_f32_16x16x32_bf16 v[136:139], v[194:197], v[84:87], v[136:139]
	ds_read_b128 v[194:197], v144 offset:8832
	s_waitcnt lgkmcnt(6)
	v_mfma_f32_16x16x32_bf16 v[132:135], v[198:201], v[88:91], v[132:135]
	v_mfma_f32_16x16x32_bf16 v[128:131], v[198:201], v[92:95], v[128:131]
	ds_read_b128 v[198:201], v144 offset:13184
	s_waitcnt lgkmcnt(6)
	v_mfma_f32_16x16x32_bf16 v[140:143], v[164:167], v[88:91], v[140:143]
	v_mfma_f32_16x16x32_bf16 v[136:139], v[164:167], v[92:95], v[136:139]
	ds_read_b128 v[164:167], v144 offset:8896
	s_waitcnt lgkmcnt(6)
	v_mfma_f32_16x16x32_bf16 v[124:127], v[168:171], v[64:67], 0
	v_mfma_f32_16x16x32_bf16 v[120:123], v[168:171], v[68:71], 0
	ds_read_b128 v[168:171], v144 offset:13248
	s_waitcnt lgkmcnt(6)
	v_mfma_f32_16x16x32_bf16 v[116:119], v[172:175], v[64:67], 0
	v_mfma_f32_16x16x32_bf16 v[112:115], v[172:175], v[68:71], 0
	s_waitcnt lgkmcnt(5)
	v_mfma_f32_16x16x32_bf16 v[124:127], v[176:179], v[72:75], v[124:127]
	v_mfma_f32_16x16x32_bf16 v[120:123], v[176:179], v[76:79], v[120:123]
	s_waitcnt lgkmcnt(4)
	v_mfma_f32_16x16x32_bf16 v[116:119], v[180:183], v[72:75], v[116:119]
	v_mfma_f32_16x16x32_bf16 v[112:115], v[180:183], v[76:79], v[112:115]
	s_waitcnt lgkmcnt(3)
	v_mfma_f32_16x16x32_bf16 v[124:127], v[194:197], v[80:83], v[124:127]
	v_mfma_f32_16x16x32_bf16 v[120:123], v[194:197], v[84:87], v[120:123]
	s_waitcnt lgkmcnt(2)
	v_mfma_f32_16x16x32_bf16 v[116:119], v[198:201], v[80:83], v[116:119]
	v_mfma_f32_16x16x32_bf16 v[112:115], v[198:201], v[84:87], v[112:115]
	s_waitcnt lgkmcnt(1)
	v_mfma_f32_16x16x32_bf16 v[124:127], v[164:167], v[88:91], v[124:127]
	v_mfma_f32_16x16x32_bf16 v[120:123], v[164:167], v[92:95], v[120:123]
	s_waitcnt lgkmcnt(0)
	v_mfma_f32_16x16x32_bf16 v[116:119], v[168:171], v[88:91], v[116:119]
	v_mfma_f32_16x16x32_bf16 v[112:115], v[168:171], v[92:95], v[112:115]
	s_cbranch_scc1 .LBB0_531
; #define LAS __attribute__((address_space(3)))
; __device__ __forceinline__ void attn_wg_task(const Frame& F, int l, int task) {
;     ...
; #pragma unroll
;                 for (int g = 0; g < 2; ++g)
; #pragma unroll
;                     for (int ab = 0; ab < 2; ++ab) {
;                         const int kk0 = 32 * g + 8 * rq + 4 * ab;
;                         const f32x4 rk = *(const LAS f32x4*)(rkb + kk0);
; #pragma unroll
;                         for (int qb = 0; qb < 2; ++qb)
; #pragma unroll
;                             for (int e = 0; e < 4; ++e) {
;                                 int rel = qi0 + qb * 16 - (kk0 + e) + relbase; rel = rel > 128 ? 128 : (rel < -128 ? -128 : rel);
;                                 const float sv = sa[qb][g][ab][e] * rk[e] + bh[rel + 128];
;                                 sa[qb][g][ab][e] = sv; mx[qb] = fmaxf(mx[qb], sv);
;                             }
;                     }
;             }
	v_add_u32_e32 v184, s2, v231
	v_add_u32_e32 v165, -1, v184
	v_min_i32_e32 v164, 0x80, v184
	v_min_i32_e32 v165, 0x80, v165
	v_lshl_add_u32 v196, v208, 2, s4
	v_lshl_add_u32 v164, v164, 2, s8
	v_lshl_add_u32 v165, v165, 2, s8
	ds_read_b128 v[172:175], v196
	ds_read_b128 v[144:147], v196 offset:16
	ds_read_b32 v164, v164 offset:512
	ds_read_b32 v165, v165 offset:512
	v_add_u32_e32 v169, 13, v184
	v_subrev_u32_e32 v181, 33, v184
	v_min_i32_e32 v169, 0x80, v169
	v_min_i32_e32 v181, 0x80, v181
	v_lshl_add_u32 v169, v169, 2, s8
	v_lshl_add_u32 v181, v181, 2, s8
	ds_read_b32 v169, v169 offset:512
	ds_read_b32 v181, v181 offset:512
	s_waitcnt lgkmcnt(2)
	v_pk_fma_f32 v[166:167], v[132:133], v[172:173], v[164:165]
	v_add_u32_e32 v164, -2, v184
	v_add_u32_e32 v165, -3, v184
	v_min_i32_e32 v164, 0x80, v164
	v_min_i32_e32 v165, 0x80, v165
	v_lshl_add_u32 v164, v164, 2, s8
	v_lshl_add_u32 v165, v165, 2, s8
	ds_read_b32 v164, v164 offset:512
	ds_read_b32 v165, v165 offset:512
	ds_read_b128 v[236:239], v196 offset:144
	v_add_u32_e32 v177, 11, v184
	v_min_i32_e32 v177, 0x80, v177
	v_lshl_add_u32 v177, v177, 2, s8
	v_max3_f32 v168, v166, s6, v167
	ds_read_b32 v177, v177 offset:512
	s_waitcnt lgkmcnt(2)
	v_pk_fma_f32 v[170:171], v[134:135], v[174:175], v[164:165]
	v_add_u32_e32 v164, 16, v184
	v_add_u32_e32 v165, 15, v184
	v_max3_f32 v176, v168, v170, v171
	v_min_i32_e32 v164, 0x80, v164
	v_min_i32_e32 v165, 0x80, v165
	v_add_u32_e32 v168, 14, v184
	v_lshl_add_u32 v164, v164, 2, s8
	v_lshl_add_u32 v165, v165, 2, s8
	v_min_i32_e32 v168, 0x80, v168
	ds_read_b32 v164, v164 offset:512
	ds_read_b32 v165, v165 offset:512
	v_lshl_add_u32 v168, v168, 2, s8
	ds_read_b32 v168, v168 offset:512
	v_subrev_u32_e32 v180, 32, v184
	v_min_i32_e32 v180, 0x80, v180
	v_lshl_add_u32 v180, v180, 2, s8
	ds_read_b32 v180, v180 offset:512
	s_waitcnt lgkmcnt(2)
	v_pk_fma_f32 v[164:165], v[128:129], v[172:173], v[164:165]
	s_waitcnt lgkmcnt(1)
	v_pk_fma_f32 v[168:169], v[130:131], v[174:175], v[168:169]
	v_max3_f32 v172, v164, s6, v165
	v_max3_f32 v178, v172, v168, v169
	v_add_u32_e32 v172, -4, v184
	v_add_u32_e32 v173, -5, v184
	v_min_i32_e32 v172, 0x80, v172
	v_min_i32_e32 v173, 0x80, v173
	v_add_u32_e32 v174, -6, v184
	v_add_u32_e32 v175, -7, v184
	v_lshl_add_u32 v172, v172, 2, s8
	v_lshl_add_u32 v173, v173, 2, s8
	v_min_i32_e32 v174, 0x80, v174
	v_min_i32_e32 v175, 0x80, v175
	ds_read_b32 v172, v172 offset:512
	ds_read_b32 v173, v173 offset:512
	v_lshl_add_u32 v174, v174, 2, s8
	v_lshl_add_u32 v175, v175, 2, s8
	ds_read_b32 v174, v174 offset:512
	ds_read_b32 v175, v175 offset:512
	v_subrev_u32_e32 v183, 35, v184
	v_min_i32_e32 v183, 0x80, v183
	v_lshl_add_u32 v183, v183, 2, s8
	ds_read_b32 v183, v183 offset:512
	s_waitcnt lgkmcnt(3)
	v_pk_fma_f32 v[172:173], v[140:141], v[144:145], v[172:173]
	s_waitcnt lgkmcnt(1)
	v_pk_fma_f32 v[174:175], v[142:143], v[146:147], v[174:175]
	v_max3_f32 v176, v176, v172, v173
	v_max3_f32 v182, v176, v174, v175
	v_add_u32_e32 v176, 12, v184
	v_min_i32_e32 v176, 0x80, v176
	v_lshl_add_u32 v176, v176, 2, s8
	ds_read_b32 v176, v176 offset:512
	v_subrev_u32_e32 v195, 17, v184
	v_min_i32_e32 v195, 0x80, v195
	v_lshl_add_u32 v195, v195, 2, s8
	ds_read_b32 v195, v195 offset:512
	s_waitcnt lgkmcnt(1)
	v_pk_fma_f32 v[144:145], v[136:137], v[144:145], v[176:177]
	v_add_u32_e32 v176, 10, v184
	v_add_u32_e32 v177, 9, v184
	v_min_i32_e32 v176, 0x80, v176
	v_min_i32_e32 v177, 0x80, v177
	v_lshl_add_u32 v176, v176, 2, s8
	v_lshl_add_u32 v177, v177, 2, s8
	ds_read_b32 v176, v176 offset:512
	ds_read_b32 v177, v177 offset:512
	v_max3_f32 v178, v178, v144, v145
	s_mov_b64 s[0:1], 0
	s_waitcnt lgkmcnt(0)
	v_pk_fma_f32 v[146:147], v[138:139], v[146:147], v[176:177]
	s_nop 0
	v_max3_f32 v197, v178, v146, v147
	ds_read_b128 v[176:179], v196 offset:128
	s_waitcnt lgkmcnt(0)
	v_pk_fma_f32 v[180:181], v[124:125], v[176:177], v[180:181]
	s_nop 0
	v_max3_f32 v194, v182, v180, v181
	v_subrev_u32_e32 v182, 34, v184
	v_min_i32_e32 v182, 0x80, v182
	v_lshl_add_u32 v182, v182, 2, s8
	ds_read_b32 v182, v182 offset:512
	s_waitcnt lgkmcnt(0)
	v_pk_fma_f32 v[182:183], v[126:127], v[178:179], v[182:183]
	s_nop 0
	v_max3_f32 v198, v194, v182, v183
	v_add_u32_e32 v194, -16, v184
	v_min_i32_e32 v194, 0x80, v194
	v_lshl_add_u32 v194, v194, 2, s8
	ds_read_b32 v194, v194 offset:512
	s_waitcnt lgkmcnt(0)
	v_pk_fma_f32 v[176:177], v[120:121], v[176:177], v[194:195]
	v_subrev_u32_e32 v194, 18, v184
	v_subrev_u32_e32 v195, 19, v184
	v_min_i32_e32 v194, 0x80, v194
	v_min_i32_e32 v195, 0x80, v195
	v_lshl_add_u32 v194, v194, 2, s8
	v_lshl_add_u32 v195, v195, 2, s8
	ds_read_b32 v194, v194 offset:512
	ds_read_b32 v195, v195 offset:512
	v_max3_f32 v197, v197, v176, v177
	s_waitcnt lgkmcnt(0)
	v_pk_fma_f32 v[178:179], v[122:123], v[178:179], v[194:195]
	v_subrev_u32_e32 v194, 36, v184
	v_subrev_u32_e32 v195, 37, v184
	v_min_i32_e32 v194, 0x80, v194
	v_min_i32_e32 v195, 0x80, v195
	v_lshl_add_u32 v194, v194, 2, s8
	v_lshl_add_u32 v195, v195, 2, s8
	ds_read_b32 v194, v194 offset:512
	ds_read_b32 v195, v195 offset:512
	v_max3_f32 v200, v197, v178, v179
	s_waitcnt lgkmcnt(0)
	v_pk_fma_f32 v[196:197], v[116:117], v[236:237], v[194:195]
	v_subrev_u32_e32 v194, 38, v184
	v_subrev_u32_e32 v195, 39, v184
	v_min_i32_e32 v194, 0x80, v194
	v_min_i32_e32 v195, 0x80, v195
	v_lshl_add_u32 v194, v194, 2, s8
	v_lshl_add_u32 v195, v195, 2, s8
	ds_read_b32 v194, v194 offset:512
	ds_read_b32 v195, v195 offset:512
	v_max3_f32 v201, v198, v196, v197
	s_waitcnt lgkmcnt(0)
	v_pk_fma_f32 v[198:199], v[118:119], v[238:239], v[194:195]
	v_subrev_u32_e32 v194, 20, v184
	v_subrev_u32_e32 v195, 21, v184
	v_min_i32_e32 v194, 0x80, v194
	v_min_i32_e32 v195, 0x80, v195
	v_lshl_add_u32 v194, v194, 2, s8
	v_lshl_add_u32 v195, v195, 2, s8
	ds_read_b32 v194, v194 offset:512
	ds_read_b32 v195, v195 offset:512
	v_max3_f32 v234, v201, v198, v199
	s_waitcnt lgkmcnt(0)
	v_pk_fma_f32 v[194:195], v[112:113], v[236:237], v[194:195]
	s_nop 0
	v_max3_f32 v235, v200, v194, v195
	v_subrev_u32_e32 v200, 22, v184
	v_subrev_u32_e32 v184, 23, v184
	v_min_i32_e32 v200, 0x80, v200
	v_min_i32_e32 v184, 0x80, v184
	v_lshl_add_u32 v200, v200, 2, s8
	v_lshl_add_u32 v184, v184, 2, s8
	ds_read_b32 v200, v200 offset:512
	ds_read_b32 v201, v184 offset:512
	s_waitcnt lgkmcnt(0)
	v_pk_fma_f32 v[200:201], v[114:115], v[238:239], v[200:201]
	s_nop 0
	v_max3_f32 v184, v235, v200, v201

; #define LAS __attribute__((address_space(3)))
; __device__ __forceinline__ f32x4 mfma16(bf16x8 a, bf16x8 b, f32x4 c) { return __builtin_amdgcn_mfma_f32_16x16x32_bf16(a, b, c, 0, 0, 0); }
; __device__ __forceinline__ float rq_max(float v) { v = fmaxf(v, __shfl_xor(v, 16)); v = fmaxf(v, __shfl_xor(v, 32)); return v; }
; __device__ __forceinline__ float fexp2(float x) { return __builtin_amdgcn_exp2f(x); }
; __device__ __forceinline__ void attn_wg_task(const Frame& F, int l, int task) {
;     ...
;             for (int qb = 0; qb < 2; ++qb) {
;                 const float mxr = rq_max(mx[qb]);
;                 const float mn = fmaxf(m_run[qb], mxr); alpha[qb] = fexp2(m_run[qb] - mn);
;                 moved = moved || (mn > m_run[qb]);
;                 float ps = 0.f;
; #pragma unroll
;                 for (int g = 0; g < 2; ++g) {
; #pragma unroll
;                     for (int ab = 0; ab < 2; ++ab)
; #pragma unroll
;                         for (int e = 0; e < 4; ++e) { const float p = fexp2(sa[qb][g][ab][e] - mn); sa[qb][g][ab][e] = p; ps += p; }
;                     Pf[qb][g] = pack8(sa[qb][g][0], sa[qb][g][1]);
;                 }
;                 l_run[qb] = l_run[qb] * alpha[qb] + ps; m_run[qb] = mn;
;             }
;             if (__any(moved)) {
; #pragma unroll
;                 for (int qb = 0; qb < 2; ++qb)
; #pragma unroll
;                     for (int db = 0; db < 8; ++db) O[qb][db] *= alpha[qb];
;             }
; #pragma unroll
;             for (int g = 0; g < 2; ++g)
; #pragma unroll
;                 for (int db = 0; db < 8; ++db) { const bf16x8 vf = *(const LAS bf16x8*)(vb + db * 16 * A_VP + g * 64); O[0][db] = mfma16(vf, Pf[0][g], O[0][db]); O[1][db] = mfma16(vf, Pf[1][g], O[1][db]); }
.LBB0_535:
	v_sub_f32_e32 v112, v166, v130
	v_exp_f32_e32 v117, v112
	v_sub_f32_e32 v112, v167, v130
	v_exp_f32_e32 v119, v112
	v_sub_f32_e32 v112, v170, v130
	v_exp_f32_e32 v133, v112
	v_sub_f32_e32 v112, v171, v130
	v_exp_f32_e32 v135, v112
	v_sub_f32_e32 v112, v172, v130
	v_exp_f32_e32 v137, v112
	v_sub_f32_e32 v112, v173, v130
	v_exp_f32_e32 v139, v112
	v_sub_f32_e32 v112, v174, v130
	v_exp_f32_e32 v141, v112
	v_sub_f32_e32 v112, v175, v130
	v_exp_f32_e32 v143, v112
	s_nop 5
	v_cvt_pk_bf16_f32 v123, v141, v143
	v_sub_f32_e32 v112, v180, v130
	v_exp_f32_e32 v167, v112
	v_sub_f32_e32 v112, v181, v130
	v_exp_f32_e32 v171, v112
	v_sub_f32_e32 v112, v182, v130
	v_exp_f32_e32 v173, v112
	v_sub_f32_e32 v112, v183, v130
	v_exp_f32_e32 v175, v112
	v_sub_f32_e32 v112, v196, v130
	v_exp_f32_e32 v181, v112
	v_sub_f32_e32 v112, v197, v130
	s_nop 1
	v_exp_f32_e32 v183, v112
	v_sub_f32_e32 v112, v198, v130
	s_nop 3
	v_exp_f32_e32 v197, v112
	v_sub_f32_e32 v112, v199, v130
	s_nop 3
	v_cvt_pk_bf16_f32 v121, v133, v135
	v_exp_f32_e32 v199, v112
	s_nop 7
	v_cvt_pk_bf16_f32 v122, v137, v139
	v_cvt_pk_bf16_f32 v120, v117, v119
	s_nop 7
	v_sub_f32_e32 v124, v168, v131
	s_nop 3
	v_exp_f32_e32 v132, v124
	v_sub_f32_e32 v124, v169, v131
	s_nop 3
	v_exp_f32_e32 v134, v124
	v_sub_f32_e32 v124, v144, v131
	v_cvt_pk_bf16_f32 v115, v197, v199
	v_cvt_pk_bf16_f32 v114, v181, v183
	v_cvt_pk_bf16_f32 v113, v173, v175
	v_cvt_pk_bf16_f32 v112, v167, v171
	v_sub_f32_e32 v116, v164, v131
	v_sub_f32_e32 v118, v165, v131
	v_exp_f32_e32 v136, v124
	v_sub_f32_e32 v124, v145, v131
	v_exp_f32_e32 v116, v116
	v_exp_f32_e32 v118, v118
	v_exp_f32_e32 v138, v124
	v_sub_f32_e32 v124, v146, v131
	v_exp_f32_e32 v140, v124
	v_sub_f32_e32 v124, v147, v131
	v_exp_f32_e32 v142, v124
	v_bfe_u32 v127, v118, 16, 1
	v_bfe_u32 v146, v116, 16, 1
	v_add3_u32 v144, v118, v127, s76
	v_bfe_u32 v127, v132, 16, 1
	s_nop 0
	v_add3_u32 v146, v116, v146, s76
	v_pk_add_f32 v[116:117], v[116:117], 0 op_sel_hi:[1,0]
	s_nop 1
	v_add3_u32 v127, v132, v127, s76
	v_pk_add_f32 v[116:117], v[118:119], v[116:117]
	s_nop 0
	v_lshrrev_b32_e32 v164, 16, v127
	s_nop 0
	v_lshrrev_b32_e32 v145, 16, v146
	v_pk_add_f32 v[116:117], v[132:133], v[116:117]
	v_cvt_pk_bf16_f32 v127, v140, v142
	v_and_or_b32 v124, v144, s75, v145
	v_sub_f32_e32 v144, v176, v131
	v_pk_add_f32 v[116:117], v[134:135], v[116:117]
	v_exp_f32_e32 v166, v144
	v_pk_add_f32 v[116:117], v[136:137], v[116:117]
	v_bfe_u32 v125, v134, 16, 1
	v_pk_add_f32 v[116:117], v[138:139], v[116:117]
	v_bfe_u32 v147, v136, 16, 1
	v_pk_add_f32 v[116:117], v[140:141], v[116:117]
	v_add3_u32 v125, v134, v125, s76
	v_pk_add_f32 v[116:117], v[142:143], v[116:117]
	v_add3_u32 v147, v136, v147, s76
	v_pk_add_f32 v[132:133], v[166:167], v[116:117]
	v_sub_f32_e32 v116, v177, v131
	v_exp_f32_e32 v170, v116
	v_sub_f32_e32 v116, v178, v131
	v_exp_f32_e32 v172, v116
	v_sub_f32_e32 v116, v179, v131
	v_exp_f32_e32 v174, v116
	v_sub_f32_e32 v116, v194, v131
	v_exp_f32_e32 v180, v116
	v_sub_f32_e32 v116, v195, v131
	v_exp_f32_e32 v182, v116
	v_sub_f32_e32 v116, v200, v131
	v_pk_add_f32 v[132:133], v[170:171], v[132:133]
	v_exp_f32_e32 v196, v116
	v_sub_f32_e32 v116, v201, v131
	v_pk_add_f32 v[132:133], v[172:173], v[132:133]
	v_exp_f32_e32 v198, v116
	v_pk_add_f32 v[132:133], v[174:175], v[132:133]
	s_nop 0
	v_pk_add_f32 v[132:133], v[180:181], v[132:133]
	s_nop 0
	v_pk_add_f32 v[132:133], v[182:183], v[132:133]
	v_bfe_u32 v119, v172, 16, 1
	s_nop 1
	v_pk_add_f32 v[132:133], v[196:197], v[132:133]
	v_bfe_u32 v126, v138, 16, 1
	s_nop 1
	v_add3_u32 v119, v172, v119, s76
	s_nop 0
	v_pk_add_f32 v[132:133], v[198:199], v[132:133]
	s_mul_i32 s0, s3, 0x4800
	v_add3_u32 v126, v138, v126, s76
	s_nop 0
	v_lshrrev_b32_e32 v138, 16, v119
	s_nop 1
	v_pk_fma_f32 v[150:151], v[150:151], v[128:129], v[132:133]
	v_add_u32_e32 v128, s0, v205
	v_cvt_pk_bf16_f32 v119, v196, v198
	v_cvt_pk_bf16_f32 v116, v166, v170
	v_lshrrev_b32_e32 v146, 16, v147
	v_and_or_b32 v125, v125, s75, v164
	v_and_or_b32 v126, v126, s75, v146
	v_bfe_u32 v137, v180, 16, 1
	s_nop 1
	v_add3_u32 v137, v180, v137, s76
	s_nop 0
	s_nop 0
	v_lshrrev_b32_e32 v136, 16, v137
	v_cvt_pk_bf16_f32 v117, v172, v174
	v_cvt_pk_bf16_f32 v118, v180, v182
	v_mov_b32_e32 v232, v131
	ds_read_b128 v[164:167], v128 offset:34816
	ds_read_b128 v[168:171], v128 offset:37120
	ds_read_b128 v[172:175], v128 offset:39424
	ds_read_b128 v[176:179], v128 offset:41728
	ds_read_b128 v[180:183], v128 offset:44032
	ds_read_b128 v[194:197], v128 offset:46336
	ds_read_b128 v[198:201], v128 offset:48640
	s_waitcnt lgkmcnt(6)
; #define LAS __attribute__((address_space(3)))
; __device__ __forceinline__ f32x4 mfma16(bf16x8 a, bf16x8 b, f32x4 c) { return __builtin_amdgcn_mfma_f32_16x16x32_bf16(a, b, c, 0, 0, 0); }
; __device__ __forceinline__ void attn_wg_task(const Frame& F, int l, int task) {
;     ...
; #pragma unroll
;             for (int g = 0; g < 2; ++g)
; #pragma unroll
;                 for (int db = 0; db < 8; ++db) { const bf16x8 vf = *(const LAS bf16x8*)(vb + db * 16 * A_VP + g * 64); O[0][db] = mfma16(vf, Pf[0][g], O[0][db]); O[1][db] = mfma16(vf, Pf[1][g], O[1][db]); }
	v_mfma_f32_16x16x32_bf16 v[32:35], v[164:167], v[120:123], v[32:35]
	v_mfma_f32_16x16x32_bf16 v[4:7], v[164:167], v[124:127], v[4:7]
	ds_read_b128 v[164:167], v128 offset:50944
	s_waitcnt lgkmcnt(6)
	v_mfma_f32_16x16x32_bf16 v[36:39], v[168:171], v[120:123], v[36:39]
	v_mfma_f32_16x16x32_bf16 v[8:11], v[168:171], v[124:127], v[8:11]
	ds_read_b128 v[168:171], v128 offset:34880
	s_waitcnt lgkmcnt(6)
	v_mfma_f32_16x16x32_bf16 v[40:43], v[172:175], v[120:123], v[40:43]
	v_mfma_f32_16x16x32_bf16 v[0:3], v[172:175], v[124:127], v[0:3]
	ds_read_b128 v[172:175], v128 offset:37184
	s_waitcnt lgkmcnt(6)
	v_mfma_f32_16x16x32_bf16 v[44:47], v[176:179], v[120:123], v[44:47]
	v_mfma_f32_16x16x32_bf16 v[12:15], v[176:179], v[124:127], v[12:15]
	ds_read_b128 v[176:179], v128 offset:39488
	s_waitcnt lgkmcnt(6)
	v_mfma_f32_16x16x32_bf16 v[48:51], v[180:183], v[120:123], v[48:51]
	v_mfma_f32_16x16x32_bf16 v[16:19], v[180:183], v[124:127], v[16:19]
	ds_read_b128 v[180:183], v128 offset:41792
	s_waitcnt lgkmcnt(6)
	v_mfma_f32_16x16x32_bf16 v[52:55], v[194:197], v[120:123], v[52:55]
	v_mfma_f32_16x16x32_bf16 v[20:23], v[194:197], v[124:127], v[20:23]
	ds_read_b128 v[194:197], v128 offset:44096
	s_waitcnt lgkmcnt(6)
	v_mfma_f32_16x16x32_bf16 v[56:59], v[198:201], v[120:123], v[56:59]
	v_mfma_f32_16x16x32_bf16 v[24:27], v[198:201], v[124:127], v[24:27]
	ds_read_b128 v[198:201], v128 offset:46400
	s_waitcnt lgkmcnt(6)
	v_mfma_f32_16x16x32_bf16 v[60:63], v[164:167], v[120:123], v[60:63]
	v_mfma_f32_16x16x32_bf16 v[28:31], v[164:167], v[124:127], v[28:31]
	ds_read_b128 v[164:167], v128 offset:48704
	s_waitcnt lgkmcnt(6)
	v_mfma_f32_16x16x32_bf16 v[32:35], v[168:171], v[112:115], v[32:35]
	v_mfma_f32_16x16x32_bf16 v[4:7], v[168:171], v[116:119], v[4:7]
	ds_read_b128 v[168:171], v128 offset:51008
	s_waitcnt lgkmcnt(6)
	v_mfma_f32_16x16x32_bf16 v[36:39], v[172:175], v[112:115], v[36:39]
	v_mfma_f32_16x16x32_bf16 v[8:11], v[172:175], v[116:119], v[8:11]
	s_waitcnt lgkmcnt(5)
	v_mfma_f32_16x16x32_bf16 v[40:43], v[176:179], v[112:115], v[40:43]
	v_mfma_f32_16x16x32_bf16 v[0:3], v[176:179], v[116:119], v[0:3]
	s_waitcnt lgkmcnt(4)
	v_mfma_f32_16x16x32_bf16 v[44:47], v[180:183], v[112:115], v[44:47]
	v_mfma_f32_16x16x32_bf16 v[12:15], v[180:183], v[116:119], v[12:15]
	s_waitcnt lgkmcnt(3)
	v_mfma_f32_16x16x32_bf16 v[48:51], v[194:197], v[112:115], v[48:51]
	v_mfma_f32_16x16x32_bf16 v[16:19], v[194:197], v[116:119], v[16:19]
	s_waitcnt lgkmcnt(2)
	v_mfma_f32_16x16x32_bf16 v[52:55], v[198:201], v[112:115], v[52:55]
	v_mfma_f32_16x16x32_bf16 v[20:23], v[198:201], v[116:119], v[20:23]
	s_waitcnt lgkmcnt(1)
	v_mfma_f32_16x16x32_bf16 v[56:59], v[164:167], v[112:115], v[56:59]
	v_mfma_f32_16x16x32_bf16 v[24:27], v[164:167], v[116:119], v[24:27]
	s_waitcnt lgkmcnt(0)
	v_mfma_f32_16x16x32_bf16 v[60:63], v[168:171], v[112:115], v[60:63]
	v_mfma_f32_16x16x32_bf16 v[28:31], v[168:171], v[116:119], v[28:31]
	s_branch .LBB0_537

; #define LAS __attribute__((address_space(3)))
; __device__ __forceinline__ f32x4 mfma16(bf16x8 a, bf16x8 b, f32x4 c) { return __builtin_amdgcn_mfma_f32_16x16x32_bf16(a, b, c, 0, 0, 0); }
; __device__ __forceinline__ void attn_wg_task(const Frame& F, int l, int task) {
;     ...
;         const int tjr = j - wch;
;         if (tjr >= 0 && tjr <= 8) {
;             const LAS unsigned char* kb = lds + A_KBUF + (j & 1) * 64 * A_KP + c * A_KP + rq * 16;
;             const LAS unsigned char* vb = lds + A_VBUF + (j & 1) * 128 * A_VP + c * A_VP + rq * 16;
;             const LAS float* rkb = (const LAS float*)(lds + A_RK) + (j & 1) * 64;
;             f32x4 sa[2][2][2];
; #pragma unroll
;             for (int g = 0; g < 2; ++g)
; #pragma unroll
;                 for (int ab = 0; ab < 2; ++ab) { f32x4 a0 = (f32x4){0.f, 0.f, 0.f, 0.f}, a1 = (f32x4){0.f, 0.f, 0.f, 0.f};
; #pragma unroll
;                     for (int ks = 0; ks < 4; ++ks) { const bf16x8 kf = *(const LAS bf16x8*)(kb + (32 * g + 16 * ab) * A_KP + ks * 64); a0 = mfma16(kf, Qf[0][ks], a0); a1 = mfma16(kf, Qf[1][ks], a1); }
;                     sa[0][g][ab] = a0; sa[1][g][ab] = a1; }
.LBB0_557:
	s_or_b64 exec, exec, s[0:1]
	s_add_i32 s5, s72, s21
	s_and_b32 s3, s21, 1
	s_cmp_gt_u32 s5, 8
	s_cbranch_scc1 .LBB0_565
	s_mul_i32 s0, s3, 0x4400
	v_add_u32_e32 v144, s0, v229
	ds_read_b128 v[164:167], v144
	ds_read_b128 v[168:171], v144 offset:4352
	ds_read_b128 v[172:175], v144 offset:64
	ds_read_b128 v[176:179], v144 offset:4416
	ds_read_b128 v[180:183], v144 offset:128
	ds_read_b128 v[194:197], v144 offset:4480
	ds_read_b128 v[198:201], v144 offset:192
	s_lshl_b32 s0, s3, 8
	s_add_i32 s4, s0, 0
	s_add_i32 s4, s4, 0x11800
	s_mov_b64 s[0:1], -1
	s_cmp_lt_u32 s5, 6
	s_waitcnt lgkmcnt(6)
	v_mfma_f32_16x16x32_bf16 v[132:135], v[164:167], v[64:67], 0
	v_mfma_f32_16x16x32_bf16 v[128:131], v[164:167], v[68:71], 0
	ds_read_b128 v[164:167], v144 offset:4544
	s_waitcnt lgkmcnt(6)
	v_mfma_f32_16x16x32_bf16 v[140:143], v[168:171], v[64:67], 0
	v_mfma_f32_16x16x32_bf16 v[136:139], v[168:171], v[68:71], 0
	ds_read_b128 v[168:171], v144 offset:8704
	s_waitcnt lgkmcnt(6)
	v_mfma_f32_16x16x32_bf16 v[132:135], v[172:175], v[72:75], v[132:135]
	v_mfma_f32_16x16x32_bf16 v[128:131], v[172:175], v[76:79], v[128:131]
	ds_read_b128 v[172:175], v144 offset:13056
	s_waitcnt lgkmcnt(6)
	v_mfma_f32_16x16x32_bf16 v[140:143], v[176:179], v[72:75], v[140:143]
	v_mfma_f32_16x16x32_bf16 v[136:139], v[176:179], v[76:79], v[136:139]
	ds_read_b128 v[176:179], v144 offset:8768
	s_waitcnt lgkmcnt(6)
	v_mfma_f32_16x16x32_bf16 v[132:135], v[180:183], v[80:83], v[132:135]
	v_mfma_f32_16x16x32_bf16 v[128:131], v[180:183], v[84:87], v[128:131]
	ds_read_b128 v[180:183], v144 offset:13120
	s_waitcnt lgkmcnt(6)
	v_mfma_f32_16x16x32_bf16 v[140:143], v[194:197], v[80:83], v[140:143]
	v_mfma_f32_16x16x32_bf16 v[136:139], v[194:197], v[84:87], v[136:139]
	ds_read_b128 v[194:197], v144 offset:8832
	s_waitcnt lgkmcnt(6)
	v_mfma_f32_16x16x32_bf16 v[132:135], v[198:201], v[88:91], v[132:135]
	v_mfma_f32_16x16x32_bf16 v[128:131], v[198:201], v[92:95], v[128:131]
	ds_read_b128 v[198:201], v144 offset:13184
	s_waitcnt lgkmcnt(6)
	v_mfma_f32_16x16x32_bf16 v[140:143], v[164:167], v[88:91], v[140:143]
	v_mfma_f32_16x16x32_bf16 v[136:139], v[164:167], v[92:95], v[136:139]
	ds_read_b128 v[164:167], v144 offset:8896
	s_waitcnt lgkmcnt(6)
	v_mfma_f32_16x16x32_bf16 v[124:127], v[168:171], v[64:67], 0
	v_mfma_f32_16x16x32_bf16 v[120:123], v[168:171], v[68:71], 0
	ds_read_b128 v[168:171], v144 offset:13248
	s_waitcnt lgkmcnt(6)
	v_mfma_f32_16x16x32_bf16 v[116:119], v[172:175], v[64:67], 0
	v_mfma_f32_16x16x32_bf16 v[112:115], v[172:175], v[68:71], 0
	s_waitcnt lgkmcnt(5)
	v_mfma_f32_16x16x32_bf16 v[124:127], v[176:179], v[72:75], v[124:127]
	v_mfma_f32_16x16x32_bf16 v[120:123], v[176:179], v[76:79], v[120:123]
	s_waitcnt lgkmcnt(4)
	v_mfma_f32_16x16x32_bf16 v[116:119], v[180:183], v[72:75], v[116:119]
	v_mfma_f32_16x16x32_bf16 v[112:115], v[180:183], v[76:79], v[112:115]
	s_waitcnt lgkmcnt(3)
	v_mfma_f32_16x16x32_bf16 v[124:127], v[194:197], v[80:83], v[124:127]
	v_mfma_f32_16x16x32_bf16 v[120:123], v[194:197], v[84:87], v[120:123]
	s_waitcnt lgkmcnt(2)
	v_mfma_f32_16x16x32_bf16 v[116:119], v[198:201], v[80:83], v[116:119]
	v_mfma_f32_16x16x32_bf16 v[112:115], v[198:201], v[84:87], v[112:115]
	s_waitcnt lgkmcnt(1)
	v_mfma_f32_16x16x32_bf16 v[124:127], v[164:167], v[88:91], v[124:127]
	v_mfma_f32_16x16x32_bf16 v[120:123], v[164:167], v[92:95], v[120:123]
	s_waitcnt lgkmcnt(0)
	v_mfma_f32_16x16x32_bf16 v[116:119], v[168:171], v[88:91], v[116:119]
	v_mfma_f32_16x16x32_bf16 v[112:115], v[168:171], v[92:95], v[112:115]
	s_cbranch_scc1 .LBB0_560
; #define LAS __attribute__((address_space(3)))
; __device__ __forceinline__ void attn_wg_task(const Frame& F, int l, int task) {
;     ...
;                     for (int ab = 0; ab < 2; ++ab) {
;                         const int kk0 = 32 * g + 8 * rq + 4 * ab;
;                         const f32x4 rk = *(const LAS f32x4*)(rkb + kk0);
; #pragma unroll
;                         for (int qb = 0; qb < 2; ++qb)
; #pragma unroll
;                             for (int e = 0; e < 4; ++e) {
;                                 int rel = qi0 + qb * 16 - (kk0 + e) + relbase; rel = rel > 128 ? 128 : (rel < -128 ? -128 : rel);
;                                 const float sv = sa[qb][g][ab][e] * rk[e] + bh[rel + 128];
;                                 sa[qb][g][ab][e] = sv; mx[qb] = fmaxf(mx[qb], sv);
;                             }
;                     }
;             }
	v_add_u32_e32 v184, s2, v231
	v_add_u32_e32 v165, -1, v184
	v_min_i32_e32 v164, 0x80, v184
	v_min_i32_e32 v165, 0x80, v165
	v_lshl_add_u32 v196, v208, 2, s4
	v_lshl_add_u32 v164, v164, 2, s20
	v_lshl_add_u32 v165, v165, 2, s20
	ds_read_b128 v[172:175], v196
	ds_read_b128 v[144:147], v196 offset:16
	ds_read_b32 v164, v164 offset:512
	ds_read_b32 v165, v165 offset:512
	v_add_u32_e32 v169, 13, v184
	v_subrev_u32_e32 v181, 33, v184
	v_min_i32_e32 v169, 0x80, v169
	v_min_i32_e32 v181, 0x80, v181
	v_lshl_add_u32 v169, v169, 2, s20
	v_lshl_add_u32 v181, v181, 2, s20
	ds_read_b32 v169, v169 offset:512
	ds_read_b32 v181, v181 offset:512
	s_waitcnt lgkmcnt(2)
	v_pk_fma_f32 v[166:167], v[132:133], v[172:173], v[164:165]
	v_add_u32_e32 v164, -2, v184
	v_add_u32_e32 v165, -3, v184
	v_min_i32_e32 v164, 0x80, v164
	v_min_i32_e32 v165, 0x80, v165
	v_lshl_add_u32 v164, v164, 2, s20
	v_lshl_add_u32 v165, v165, 2, s20
	ds_read_b32 v164, v164 offset:512
	ds_read_b32 v165, v165 offset:512
	ds_read_b128 v[236:239], v196 offset:144
	v_add_u32_e32 v177, 11, v184
	v_min_i32_e32 v177, 0x80, v177
	v_lshl_add_u32 v177, v177, 2, s20
	v_max3_f32 v168, v166, s7, v167
	ds_read_b32 v177, v177 offset:512
	s_waitcnt lgkmcnt(2)
	v_pk_fma_f32 v[170:171], v[134:135], v[174:175], v[164:165]
	v_add_u32_e32 v164, 16, v184
	v_add_u32_e32 v165, 15, v184
	v_max3_f32 v176, v168, v170, v171
	v_min_i32_e32 v164, 0x80, v164
	v_min_i32_e32 v165, 0x80, v165
	v_add_u32_e32 v168, 14, v184
	v_lshl_add_u32 v164, v164, 2, s20
	v_lshl_add_u32 v165, v165, 2, s20
	v_min_i32_e32 v168, 0x80, v168
	ds_read_b32 v164, v164 offset:512
	ds_read_b32 v165, v165 offset:512
	v_lshl_add_u32 v168, v168, 2, s20
	ds_read_b32 v168, v168 offset:512
	v_subrev_u32_e32 v180, 32, v184
	v_min_i32_e32 v180, 0x80, v180
	v_lshl_add_u32 v180, v180, 2, s20
	ds_read_b32 v180, v180 offset:512
	s_waitcnt lgkmcnt(2)
	v_pk_fma_f32 v[164:165], v[128:129], v[172:173], v[164:165]
	s_waitcnt lgkmcnt(1)
	v_pk_fma_f32 v[168:169], v[130:131], v[174:175], v[168:169]
	v_max3_f32 v172, v164, s7, v165
	v_max3_f32 v178, v172, v168, v169
	v_add_u32_e32 v172, -4, v184
	v_add_u32_e32 v173, -5, v184
	v_min_i32_e32 v172, 0x80, v172
	v_min_i32_e32 v173, 0x80, v173
	v_add_u32_e32 v174, -6, v184
	v_add_u32_e32 v175, -7, v184
	v_lshl_add_u32 v172, v172, 2, s20
	v_lshl_add_u32 v173, v173, 2, s20
	v_min_i32_e32 v174, 0x80, v174
	v_min_i32_e32 v175, 0x80, v175
	ds_read_b32 v172, v172 offset:512
	ds_read_b32 v173, v173 offset:512
	v_lshl_add_u32 v174, v174, 2, s20
	v_lshl_add_u32 v175, v175, 2, s20
	ds_read_b32 v174, v174 offset:512
	ds_read_b32 v175, v175 offset:512
	v_subrev_u32_e32 v183, 35, v184
	v_min_i32_e32 v183, 0x80, v183
	v_lshl_add_u32 v183, v183, 2, s20
	ds_read_b32 v183, v183 offset:512
	s_waitcnt lgkmcnt(3)
	v_pk_fma_f32 v[172:173], v[140:141], v[144:145], v[172:173]
	s_waitcnt lgkmcnt(1)
	v_pk_fma_f32 v[174:175], v[142:143], v[146:147], v[174:175]
	v_max3_f32 v176, v176, v172, v173
	v_max3_f32 v182, v176, v174, v175
	v_add_u32_e32 v176, 12, v184
	v_min_i32_e32 v176, 0x80, v176
	v_lshl_add_u32 v176, v176, 2, s20
	ds_read_b32 v176, v176 offset:512
	v_subrev_u32_e32 v195, 17, v184
	v_min_i32_e32 v195, 0x80, v195
	v_lshl_add_u32 v195, v195, 2, s20
	ds_read_b32 v195, v195 offset:512
	s_waitcnt lgkmcnt(1)
	v_pk_fma_f32 v[144:145], v[136:137], v[144:145], v[176:177]
	v_add_u32_e32 v176, 10, v184
	v_add_u32_e32 v177, 9, v184
	v_min_i32_e32 v176, 0x80, v176
	v_min_i32_e32 v177, 0x80, v177
	v_lshl_add_u32 v176, v176, 2, s20
	v_lshl_add_u32 v177, v177, 2, s20
	ds_read_b32 v176, v176 offset:512
	ds_read_b32 v177, v177 offset:512
	v_max3_f32 v178, v178, v144, v145
	s_mov_b64 s[0:1], 0
	s_waitcnt lgkmcnt(0)
	v_pk_fma_f32 v[146:147], v[138:139], v[146:147], v[176:177]
	s_nop 0
	v_max3_f32 v197, v178, v146, v147
	ds_read_b128 v[176:179], v196 offset:128
	s_waitcnt lgkmcnt(0)
	v_pk_fma_f32 v[180:181], v[124:125], v[176:177], v[180:181]
	s_nop 0
	v_max3_f32 v194, v182, v180, v181
	v_subrev_u32_e32 v182, 34, v184
	v_min_i32_e32 v182, 0x80, v182
	v_lshl_add_u32 v182, v182, 2, s20
	ds_read_b32 v182, v182 offset:512
	s_waitcnt lgkmcnt(0)
	v_pk_fma_f32 v[182:183], v[126:127], v[178:179], v[182:183]
	s_nop 0
	v_max3_f32 v198, v194, v182, v183
	v_add_u32_e32 v194, -16, v184
	v_min_i32_e32 v194, 0x80, v194
	v_lshl_add_u32 v194, v194, 2, s20
	ds_read_b32 v194, v194 offset:512
	s_waitcnt lgkmcnt(0)
	v_pk_fma_f32 v[176:177], v[120:121], v[176:177], v[194:195]
	v_subrev_u32_e32 v194, 18, v184
	v_subrev_u32_e32 v195, 19, v184
	v_min_i32_e32 v194, 0x80, v194
	v_min_i32_e32 v195, 0x80, v195
	v_lshl_add_u32 v194, v194, 2, s20
	v_lshl_add_u32 v195, v195, 2, s20
	ds_read_b32 v194, v194 offset:512
	ds_read_b32 v195, v195 offset:512
	v_max3_f32 v197, v197, v176, v177
	s_waitcnt lgkmcnt(0)
	v_pk_fma_f32 v[178:179], v[122:123], v[178:179], v[194:195]
	v_subrev_u32_e32 v194, 36, v184
	v_subrev_u32_e32 v195, 37, v184
	v_min_i32_e32 v194, 0x80, v194
	v_min_i32_e32 v195, 0x80, v195
	v_lshl_add_u32 v194, v194, 2, s20
	v_lshl_add_u32 v195, v195, 2, s20
	ds_read_b32 v194, v194 offset:512
	ds_read_b32 v195, v195 offset:512
	v_max3_f32 v200, v197, v178, v179
	s_waitcnt lgkmcnt(0)
	v_pk_fma_f32 v[196:197], v[116:117], v[236:237], v[194:195]
	v_subrev_u32_e32 v194, 38, v184
	v_subrev_u32_e32 v195, 39, v184
	v_min_i32_e32 v194, 0x80, v194
	v_min_i32_e32 v195, 0x80, v195
	v_lshl_add_u32 v194, v194, 2, s20
	v_lshl_add_u32 v195, v195, 2, s20
	ds_read_b32 v194, v194 offset:512
	ds_read_b32 v195, v195 offset:512
	v_max3_f32 v201, v198, v196, v197
	s_waitcnt lgkmcnt(0)
	v_pk_fma_f32 v[198:199], v[118:119], v[238:239], v[194:195]
	v_subrev_u32_e32 v194, 20, v184
	v_subrev_u32_e32 v195, 21, v184
	v_min_i32_e32 v194, 0x80, v194
	v_min_i32_e32 v195, 0x80, v195
	v_lshl_add_u32 v194, v194, 2, s20
	v_lshl_add_u32 v195, v195, 2, s20
	ds_read_b32 v194, v194 offset:512
	ds_read_b32 v195, v195 offset:512
	v_max3_f32 v234, v201, v198, v199
	s_waitcnt lgkmcnt(0)
	v_pk_fma_f32 v[194:195], v[112:113], v[236:237], v[194:195]
	s_nop 0
	v_max3_f32 v235, v200, v194, v195
	v_subrev_u32_e32 v200, 22, v184
	v_subrev_u32_e32 v184, 23, v184
	v_min_i32_e32 v200, 0x80, v200
	v_min_i32_e32 v184, 0x80, v184
	v_lshl_add_u32 v200, v200, 2, s20
	v_lshl_add_u32 v184, v184, 2, s20
	ds_read_b32 v200, v200 offset:512
	ds_read_b32 v201, v184 offset:512
	s_waitcnt lgkmcnt(0)
	v_pk_fma_f32 v[200:201], v[114:115], v[238:239], v[200:201]
	s_nop 0
	v_max3_f32 v184, v235, v200, v201
